# baseline (speedup 1.0000x reference)
.LBB0_5:
	s_or_b64 exec, exec, s[10:11]
	s_and_saveexec_b64 s[0:1], vcc
	ds_write_b128 v11, v[2:5] offset:16384
	s_or_b64 exec, exec, s[0:1]
	s_ashr_i32 s0, s14, 16
	s_add_i32 s3, s3, s0
	v_cmp_gt_i32_e32 vcc, s3, v10
	v_mov_b32_e32 v2, 0
	s_waitcnt lgkmcnt(0)
	s_sub_u32 s26, 0x1ff, s2
	s_mul_i32 s26, s26, 3
	s_lshr_b32 s26, s26, 5
	s_min_u32 s26, s26, 64
	s_cmp_eq_u32 s26, 0
	s_cbranch_scc1 .Lhold_done
